# baseline (speedup 1.0000x reference)
.LBB0_11:
	s_or_b64 exec, exec, s[6:7]
	v_mov_b32_e32 v2, v0
	s_waitcnt vmcnt(14)
	v_cvt_pkrtz_f16_f32 v66, v66, v67
	v_bfe_u32 v17, v2, 1, 3
	v_lshrrev_b32_e32 v103, 5, v2
	v_ashrrev_i32_e32 v102, 4, v2
	v_bitop3_b32 v17, v17, v103, 7 bitop3:0x78
	v_lshlrev_b32_e32 v103, 3, v2
	v_lshlrev_b32_e32 v16, 7, v102
	v_lshlrev_b32_e32 v17, 4, v17
	v_and_b32_e32 v104, 8, v103
	v_or3_b32 v104, v16, v17, v104
	v_cvt_pkrtz_f16_f32 v16, v70, v71
	v_cvt_pkrtz_f16_f32 v17, v72, v73
	v_cvt_pkrtz_f16_f32 v67, v68, v69
	ds_write2st64_b64 v104, v[16:17], v[66:67] offset1:8
	s_waitcnt vmcnt(11)
	v_cvt_pkrtz_f16_f32 v16, v90, v91
	v_cvt_pkrtz_f16_f32 v17, v92, v93
	s_waitcnt vmcnt(10)
	v_cvt_pkrtz_f16_f32 v66, v82, v83
	v_cvt_pkrtz_f16_f32 v67, v84, v85
	ds_write2st64_b64 v104, v[16:17], v[66:67] offset0:16 offset1:24
	s_waitcnt vmcnt(9)
	v_cvt_pkrtz_f16_f32 v16, v98, v99
	v_cvt_pkrtz_f16_f32 v17, v100, v101
	s_waitcnt vmcnt(8)
	v_cvt_pkrtz_f16_f32 v66, v94, v95
	v_cvt_pkrtz_f16_f32 v67, v96, v97
	ds_write2st64_b64 v104, v[16:17], v[66:67] offset0:32 offset1:40
	v_bfe_u32 v2, v2, 3, 1
	v_lshlrev_b32_e32 v16, 6, v102
	v_mad_u32_u24 v2, v2, s86, v16
	v_and_or_b32 v2, v103, 56, v2
	v_cvt_pkrtz_f16_f32 v12, v182, v183
	v_cvt_pkrtz_f16_f32 v13, v184, v185
	v_cvt_pkrtz_f16_f32 v8, v186, v187
	v_cvt_pkrtz_f16_f32 v9, v188, v189
	ds_write2st64_b64 v2, v[12:13], v[8:9] offset0:48 offset1:52
	v_mov_b32_e32 v2, v229
	s_waitcnt vmcnt(7)
	v_pk_mul_f32 v[10:11], v[86:87], s[78:79] op_sel_hi:[1,0]
	v_lshlrev_b32_e32 v8, 3, v2
	v_ashrrev_i32_e32 v14, 4, v2
	v_and_b32_e32 v15, 8, v8
	v_pk_mul_f32 v[8:9], v[88:89], s[78:79] op_sel_hi:[1,0]
	v_cvt_pkrtz_f16_f32 v10, v10, v11
	v_cvt_pkrtz_f16_f32 v11, v8, v9
	v_xor_b32_e32 v9, v14, v2
	v_lshlrev_b32_e32 v9, 3, v9
	v_lshl_add_u32 v8, v14, 7, s79
	v_and_b32_e32 v9, 0x70, v9
	v_add3_u32 v16, v8, v9, v15
	v_add_u32_e32 v17, 4, v14
	s_waitcnt vmcnt(6)
	v_pk_mul_f32 v[8:9], v[76:77], s[78:79] op_sel_hi:[1,0]
	v_pk_mul_f32 v[12:13], v[74:75], s[78:79] op_sel_hi:[1,0]
	v_cvt_pkrtz_f16_f32 v12, v12, v13
	v_cvt_pkrtz_f16_f32 v13, v8, v9
	v_xor_b32_e32 v9, v17, v2
	v_lshlrev_b32_e32 v9, 3, v9
	v_lshl_add_u32 v8, v17, 7, s79
	v_and_b32_e32 v9, 0x70, v9
	v_add3_u32 v8, v8, v9, v15
	ds_write_b64 v8, v[12:13] offset:41216
	v_add_u32_e32 v17, 8, v14
	s_waitcnt vmcnt(5)
	v_pk_mul_f32 v[8:9], v[80:81], s[78:79] op_sel_hi:[1,0]
	v_pk_mul_f32 v[12:13], v[78:79], s[78:79] op_sel_hi:[1,0]
	v_cvt_pkrtz_f16_f32 v12, v12, v13
	v_cvt_pkrtz_f16_f32 v13, v8, v9
	v_xor_b32_e32 v9, v17, v2
	v_lshlrev_b32_e32 v9, 3, v9
	v_lshl_add_u32 v8, v17, 7, s79
	v_and_b32_e32 v9, 0x70, v9
	v_add3_u32 v8, v8, v9, v15
	ds_write_b64 v8, v[12:13] offset:41216
	v_add_u32_e32 v17, 12, v14
	s_waitcnt vmcnt(4)
	v_pk_mul_f32 v[8:9], v[60:61], s[78:79] op_sel_hi:[1,0]
	v_pk_mul_f32 v[12:13], v[58:59], s[78:79] op_sel_hi:[1,0]
	v_cvt_pkrtz_f16_f32 v12, v12, v13
	v_cvt_pkrtz_f16_f32 v13, v8, v9
	v_xor_b32_e32 v9, v17, v2
	v_lshlrev_b32_e32 v9, 3, v9
	v_lshl_add_u32 v8, v17, 7, s79
	v_and_b32_e32 v9, 0x70, v9
	v_add3_u32 v8, v8, v9, v15
	ds_write_b64 v8, v[12:13] offset:41216
	s_waitcnt vmcnt(3)
	v_pk_mul_f32 v[8:9], v[64:65], s[78:79] op_sel_hi:[1,0]
	v_pk_mul_f32 v[12:13], v[62:63], s[78:79] op_sel_hi:[1,0]
	v_cvt_pkrtz_f16_f32 v12, v12, v13
	v_cvt_pkrtz_f16_f32 v13, v8, v9
	v_add_u32_e32 v8, 0x100, v16
	ds_write2st64_b64 v8, v[10:11], v[12:13] offset0:80 offset1:84
	v_add_u32_e32 v12, 20, v14
	s_waitcnt vmcnt(2)
	v_pk_mul_f32 v[8:9], v[52:53], s[78:79] op_sel_hi:[1,0]
	v_pk_mul_f32 v[10:11], v[50:51], s[78:79] op_sel_hi:[1,0]
	s_andn2_b64 vcc, exec, s[4:5]
	v_cvt_pkrtz_f16_f32 v10, v10, v11
	v_cvt_pkrtz_f16_f32 v11, v8, v9
	v_xor_b32_e32 v9, v12, v2
	v_lshlrev_b32_e32 v9, 3, v9
	v_lshl_add_u32 v8, v12, 7, s79
	v_and_b32_e32 v9, 0x70, v9
	v_add3_u32 v8, v8, v9, v15
	ds_write_b64 v8, v[10:11] offset:41216
	v_add_u32_e32 v12, 24, v14
	s_waitcnt vmcnt(1)
	v_pk_mul_f32 v[8:9], v[56:57], s[78:79] op_sel_hi:[1,0]
	v_pk_mul_f32 v[10:11], v[54:55], s[78:79] op_sel_hi:[1,0]
	s_mov_b32 s94, s11
	v_cvt_pkrtz_f16_f32 v10, v10, v11
	v_cvt_pkrtz_f16_f32 v11, v8, v9
	v_xor_b32_e32 v9, v12, v2
	v_lshlrev_b32_e32 v9, 3, v9
	v_lshl_add_u32 v8, v12, 7, s79
	v_and_b32_e32 v9, 0x70, v9
	v_add3_u32 v8, v8, v9, v15
	ds_write_b64 v8, v[10:11] offset:41216
	s_waitcnt vmcnt(0)
	v_pk_mul_f32 v[6:7], v[180:181], s[78:79] op_sel_hi:[1,0]
	v_pk_mul_f32 v[4:5], v[178:179], s[78:79] op_sel_hi:[1,0]
	v_cvt_pkrtz_f16_f32 v4, v4, v5
	v_cvt_pkrtz_f16_f32 v5, v6, v7
	v_add_u32_e32 v8, 28, v14
	v_xor_b32_e32 v2, v8, v2
	v_lshlrev_b32_e32 v2, 3, v2
	v_lshl_add_u32 v6, v8, 7, s79
	v_and_b32_e32 v2, 0x70, v2
	v_add3_u32 v2, v6, v2, v15
	s_mov_b32 s91, s13
	s_mov_b32 s89, s14
	s_mov_b32 s93, s12
	s_mov_b32 s92, s10
	ds_write_b64 v2, v[4:5] offset:41216
	s_waitcnt lgkmcnt(0)
	s_barrier
	s_cbranch_vccnz .LBB0_13
	ds_read_b128 v[4:7], v235
	s_waitcnt lgkmcnt(0)
	v_readfirstlane_b32 s4, v6
	v_readfirstlane_b32 s92, v4
	v_readfirstlane_b32 s93, v5
	s_and_b32 s89, s4, 0xffff
	s_ashr_i32 s91, s4, 16
	v_readfirstlane_b32 s94, v7
